# v072
# baseline (speedup 1.0000x reference)
_Z9lstm_diag8DiagArgs:
	s_load_dwordx4 s[12:15], s[0:1], 0x18
	s_load_dwordx4 s[8:11], s[0:1], 0x0
	s_load_dwordx2 s[6:7], s[0:1], 0x30
	s_mov_b64 s[4:5], -1
	s_waitcnt lgkmcnt(0)
	s_cmp_lt_i32 s2, s14
	s_cbranch_scc1 .LBB2_7
	s_load_dword s3, s[0:1], 0x28
	s_sub_i32 s4, s2, s14
	v_lshl_or_b32 v2, s4, 9, v0
	s_waitcnt lgkmcnt(0)
	s_sub_i32 s3, s3, s15
	s_lshl_b32 s3, s3, 19
	v_cmp_gt_u32_e32 vcc, s3, v2
	s_and_saveexec_b64 s[6:7], vcc
	s_cbranch_execz .LBB2_6
	s_load_dword s4, s[0:1], 0x38
	s_load_dwordx2 s[16:17], s[0:1], 0x10
	s_lshl_b32 s5, s14, 9
	s_sub_i32 s24, 0, s5
	s_lshl_b32 s18, s14, 10
	s_waitcnt lgkmcnt(0)
	s_lshl_b32 s5, s4, 10
	s_sub_i32 s25, s5, s18
	s_lshl_b32 s5, s4, 14
	s_lshl_b32 s14, s14, 14
	s_lshl_b32 s4, s4, 9
	s_movk_i32 s20, 0xf000
	s_mov_b32 s22, 0xff000000
	v_lshl_or_b32 v1, s2, 9, v0
	v_lshlrev_b32_e32 v24, 4, v2
	s_sub_i32 s14, s5, s14
	s_sub_i32 s26, s4, s18
	s_mov_b64 s[18:19], 0
	s_movk_i32 s27, 0x400
	v_mov_b32_e32 v19, 0
	s_mov_b32 s21, -1
	s_mov_b32 s23, -1
	s_mov_b32 s28, 0xff000000
	v_mov_b32_e32 v25, 0xc4b8aa3b
	v_mov_b32_e32 v26, 0xc538aa3b
	s_mov_b32 s29, 0xc3e00000
	v_mov_b32_e32 v27, 0x43e00000
	s_branch .LBB2_4

.LBB2_7:
	s_andn2_b64 vcc, exec, s[4:5]
	s_cbranch_vccnz .LBB2_96
	s_mov_b64 s[0:1], s[6:7]
	s_ashr_i32 s16, s2, 3
	s_lshl_b32 s3, s12, 3
	s_cmp_lt_i32 s16, s3
	s_cselect_b64 s[4:5], -1, 0
	s_cmp_ge_i32 s16, s3
	v_readfirstlane_b32 s33, v0
	s_cbranch_scc1 .LBB2_20
	s_lshl_b32 s3, s2, 1
	s_and_b32 s3, s3, 14
	s_mul_i32 s3, s12, s3
	s_ashr_i32 s6, s2, 5
	s_add_i32 s3, s3, s6
	s_ashr_i32 s6, s3, 1
	s_and_b32 s6, s6, -8
	s_waitcnt lgkmcnt(0)
	s_lshr_b32 s0, s0, s6
	s_and_b32 s30, s0, 7
	s_bfe_u32 s34, s0, 0x50003
	s_cmp_eq_u32 s30, 0
	s_cselect_b64 s[6:7], -1, 0
	s_cmp_eq_u32 s34, 0
	s_cselect_b64 s[10:11], -1, 0
	s_cmp_lg_u32 s30, 0
	s_cbranch_scc0 .LBB2_11
	s_lshl_b32 s12, s34, 21
	s_lshl_b32 s0, s30, 22
	s_and_b32 s12, s12, 0x200000
	s_or_b32 s0, s0, s12
	s_add_i32 s12, s0, 0x7c00000
	s_cbranch_execz .LBB2_12
	s_branch .LBB2_13
